# one static s_setprio 1 for waves 0-3 at kernel entry, all per-segment s_setprio removed (on top of v59)
# speedup vs baseline: 1.0129x; 1.0059x over previous
_Z3fwd4Args:
	s_mov_b32 s96, s2
	s_load_dwordx4 s[44:47], s[0:1], 0xc8
	s_add_u32 s2, s0, 0xd8
	s_addc_u32 s3, s1, 0
	v_readfirstlane_b32 s10, v0
	v_writelane_b32 v252, s2, 0
	s_nop 1
	v_writelane_b32 v252, s3, 1
	s_movk_i32 s2, 0x200
	v_cmp_gt_u32_e32 vcc, s2, v0
	s_and_saveexec_b64 s[4:5], vcc
	v_lshl_add_u32 v1, v0, 2, 0
	v_add_u32_e32 v1, 0x24c00, v1
	v_mov_b32_e32 v2, 0
	ds_write_b32 v1, v2
	s_or_b64 exec, exec, s[4:5]
	s_lshr_b32 s4, s10, 6
	s_cmp_ge_u32 s4, 4
	s_cbranch_scc1 .Lprio_static_done
	s_setprio 1
